# v11 + hand-written adaLN-modulation sub-phase of the prologue (16-byte weight loads, ring of 16 in flight per lane)
# baseline (speedup 1.0000x reference)
.LBB0_20:
	s_or_b64 exec, exec, s[8:9]
	v_readlane_b32 s0, v251, 3
	s_cmpk_gt_i32 s0, 0x2ff
	v_and_b32_e32 v1, 31, v130
	s_waitcnt lgkmcnt(0)
	s_barrier
	s_cbranch_scc1 .LBB0_28
	v_readlane_b32 s0, v251, 3
	s_lshr_b32 s1, s22, 6
	v_and_b32_e32 v118, 7, v130
	v_bfe_u32 v119, v130, 3, 3
	s_mov_b32 s6, 0x180000
	v_mul_u32_u24_e32 v108, s6, v119
	v_lshl_add_u32 v108, v118, 4, v108
	s_lshl_b32 s6, s1, 3
	v_add_u32_e32 v119, s6, v119
	v_lshlrev_b32_e32 v109, 7, v119
	v_add_u32_e32 v110, 0x10000, v109
	s_movk_i32 s6, 0x480
	v_mul_u32_u24_e32 v111, s6, v119
	v_lshl_add_u32 v111, v118, 4, v111
	v_add_u32_e32 v111, 0x12000, v111
	s_movk_i32 s6, 0x120
	v_cmp_gt_u32_e32 vcc, s6, v130
	v_subrev_u32_e32 v118, s6, v130
	v_cndmask_b32_e32 v120, v118, v130, vcc
	v_lshlrev_b32_e32 v112, 2, v120
	v_add_u32_e32 v112, 0x12000, v112
	v_add_u32_e32 v113, 0x9000, v112
	v_lshrrev_b32_e32 v118, 5, v120
	s_mov_b32 s6, 0xc000
	v_mul_u32_u24_e32 v114, s6, v118
	v_and_b32_e32 v118, 31, v120
	v_lshlrev_b32_e32 v116, 2, v118
	v_add_u32_e32 v114, v114, v116
	s_mov_b32 s4, 0
	s_mov_b32 s29, s0
	s_cmpk_ge_u32 s29, 0x180
	s_cselect_b32 s5, 1, 0
	s_cselect_b32 s6, 0x180, 0
	s_sub_i32 s6, s29, s6
	s_lshl_b32 s6, s6, 7
	s_mul_i32 s7, s5, 0x6000000
	s_add_u32 s34, s84, s7
	s_addc_u32 s35, s85, 0
	s_add_u32 s34, s34, s6
	s_addc_u32 s35, s35, 0
	s_mul_i32 s7, s1, 0xc00000
	s_add_u32 s34, s34, s7
	s_addc_u32 s35, s35, 0
	s_mov_b64 s[24:25], s[34:35]
	global_load_dwordx4 v[132:135], v108, s[24:25] nt
	s_add_u32 s24, s24, 0xc000
	s_addc_u32 s25, s25, 0
	global_load_dwordx4 v[136:139], v108, s[24:25] nt
	s_add_u32 s24, s24, 0xc000
	s_addc_u32 s25, s25, 0
	global_load_dwordx4 v[140:143], v108, s[24:25] nt
	s_add_u32 s24, s24, 0xc000
	s_addc_u32 s25, s25, 0
	global_load_dwordx4 v[144:147], v108, s[24:25] nt
	s_add_u32 s24, s24, 0xc000
	s_addc_u32 s25, s25, 0
	global_load_dwordx4 v[148:151], v108, s[24:25] nt
	s_add_u32 s24, s24, 0xc000
	s_addc_u32 s25, s25, 0
	global_load_dwordx4 v[152:155], v108, s[24:25] nt
	s_add_u32 s24, s24, 0xc000
	s_addc_u32 s25, s25, 0
	global_load_dwordx4 v[156:159], v108, s[24:25] nt
	s_add_u32 s24, s24, 0xc000
	s_addc_u32 s25, s25, 0
	global_load_dwordx4 v[160:163], v108, s[24:25] nt
	s_add_u32 s24, s24, 0xc000
	s_addc_u32 s25, s25, 0
	global_load_dwordx4 v[164:167], v108, s[24:25] nt
	s_add_u32 s24, s24, 0xc000
	s_addc_u32 s25, s25, 0
	global_load_dwordx4 v[168:171], v108, s[24:25] nt
	s_add_u32 s24, s24, 0xc000
	s_addc_u32 s25, s25, 0
	global_load_dwordx4 v[172:175], v108, s[24:25] nt
	s_add_u32 s24, s24, 0xc000
	s_addc_u32 s25, s25, 0
	global_load_dwordx4 v[176:179], v108, s[24:25] nt
	s_add_u32 s24, s24, 0xc000
	s_addc_u32 s25, s25, 0
	global_load_dwordx4 v[180:183], v108, s[24:25] nt
	s_add_u32 s24, s24, 0xc000
	s_addc_u32 s25, s25, 0
	global_load_dwordx4 v[184:187], v108, s[24:25] nt
	s_add_u32 s24, s24, 0xc000
	s_addc_u32 s25, s25, 0
	global_load_dwordx4 v[188:191], v108, s[24:25] nt
	s_add_u32 s24, s24, 0xc000
	s_addc_u32 s25, s25, 0
	global_load_dwordx4 v[192:195], v108, s[24:25] nt
	s_add_u32 s24, s24, 0xc000
	s_addc_u32 s25, s25, 0
.Lada_item:
	s_lshl_b32 s6, s4, 8
	s_add_i32 s29, s0, s6
	s_cmpk_ge_u32 s29, 0x180
	s_cselect_b32 s5, 1, 0
	s_cselect_b32 s6, 0x180, 0
	s_sub_i32 s6, s29, s6
	s_lshl_b32 s6, s6, 7
	s_mul_i32 s7, s5, 0x6c000
	s_add_u32 s30, s20, s7
	s_addc_u32 s31, s21, 0
	s_add_u32 s30, s30, s6
	s_addc_u32 s31, s31, 0
	s_add_u32 s30, s30, 0x10000
	s_addc_u32 s31, s31, 0
	s_mul_i32 s7, s5, 0xc000
	s_add_u32 s32, s86, s7
	s_addc_u32 s33, s87, 0
	s_add_u32 s32, s32, s6
	s_addc_u32 s33, s33, 0
	global_load_dword v115, v116, s[32:33]
	s_min_u32 s6, s4, 1
	s_add_i32 s6, s6, 1
	s_lshl_b32 s6, s6, 8
	s_add_i32 s29, s0, s6
	s_cmpk_ge_u32 s29, 0x180
	s_cselect_b32 s5, 1, 0
	s_cselect_b32 s6, 0x180, 0
	s_sub_i32 s6, s29, s6
	s_lshl_b32 s6, s6, 7
	s_mul_i32 s7, s5, 0x6000000
	s_add_u32 s26, s84, s7
	s_addc_u32 s27, s85, 0
	s_add_u32 s26, s26, s6
	s_addc_u32 s27, s27, 0
	s_mul_i32 s7, s1, 0xc00000
	s_add_u32 s26, s26, s7
	s_addc_u32 s27, s27, 0
	v_mov_b32_e32 v196, 0
	v_mov_b32_e32 v197, 0
	v_mov_b32_e32 v198, 0
	v_mov_b32_e32 v199, 0
	v_mov_b32_e32 v200, 0
	v_mov_b32_e32 v201, 0
	v_mov_b32_e32 v202, 0
	v_mov_b32_e32 v203, 0
	v_mov_b32_e32 v204, 0
	v_mov_b32_e32 v205, 0
	v_mov_b32_e32 v206, 0
	v_mov_b32_e32 v207, 0
	v_mov_b32_e32 v208, 0
	v_mov_b32_e32 v209, 0
	v_mov_b32_e32 v210, 0
	v_mov_b32_e32 v211, 0
	v_mov_b32_e32 v212, 0
	v_mov_b32_e32 v213, 0
	v_mov_b32_e32 v214, 0
	v_mov_b32_e32 v215, 0
	v_mov_b32_e32 v216, 0
	v_mov_b32_e32 v217, 0
	v_mov_b32_e32 v218, 0
	v_mov_b32_e32 v219, 0
	v_mov_b32_e32 v220, 0
	v_mov_b32_e32 v221, 0
	v_mov_b32_e32 v222, 0
	v_mov_b32_e32 v223, 0
	v_mov_b32_e32 v224, 0
	v_mov_b32_e32 v225, 0
	v_mov_b32_e32 v226, 0
	v_mov_b32_e32 v227, 0
	v_mov_b32_e32 v228, 0
	v_mov_b32_e32 v229, 0
	v_mov_b32_e32 v230, 0
	v_mov_b32_e32 v231, 0
	ds_read_b128 v[36:39], v109 offset:0
	ds_read_b128 v[40:43], v109 offset:8192
	ds_read_b128 v[44:47], v109 offset:16384
	ds_read_b128 v[48:51], v109 offset:24576
	ds_read_b128 v[52:55], v109 offset:32768
	ds_read_b128 v[56:59], v109 offset:40960
	ds_read_b128 v[60:63], v109 offset:49152
	ds_read_b128 v[64:67], v109 offset:57344
	ds_read_b128 v[68:71], v110 offset:0
	ds_read_b128 v[72:75], v109 offset:16
	ds_read_b128 v[76:79], v109 offset:8208
	ds_read_b128 v[80:83], v109 offset:16400
	ds_read_b128 v[84:87], v109 offset:24592
	ds_read_b128 v[88:91], v109 offset:32784
	ds_read_b128 v[92:95], v109 offset:40976
	ds_read_b128 v[96:99], v109 offset:49168
	ds_read_b128 v[100:103], v109 offset:57360
	ds_read_b128 v[104:107], v110 offset:16
	s_waitcnt lgkmcnt(9)
	s_waitcnt vmcnt(16)
	v_fmac_f32_e32 v196, v36, v132
	v_fmac_f32_e32 v197, v36, v133
	v_fmac_f32_e32 v198, v36, v134
	v_fmac_f32_e32 v199, v36, v135
	v_fmac_f32_e32 v200, v40, v132
	v_fmac_f32_e32 v201, v40, v133
	v_fmac_f32_e32 v202, v40, v134
	v_fmac_f32_e32 v203, v40, v135
	v_fmac_f32_e32 v204, v44, v132
	v_fmac_f32_e32 v205, v44, v133
	v_fmac_f32_e32 v206, v44, v134
	v_fmac_f32_e32 v207, v44, v135
	v_fmac_f32_e32 v208, v48, v132
	v_fmac_f32_e32 v209, v48, v133
	v_fmac_f32_e32 v210, v48, v134
	v_fmac_f32_e32 v211, v48, v135
	v_fmac_f32_e32 v212, v52, v132
	v_fmac_f32_e32 v213, v52, v133
	v_fmac_f32_e32 v214, v52, v134
	v_fmac_f32_e32 v215, v52, v135
	v_fmac_f32_e32 v216, v56, v132
	v_fmac_f32_e32 v217, v56, v133
	v_fmac_f32_e32 v218, v56, v134
	v_fmac_f32_e32 v219, v56, v135
	v_fmac_f32_e32 v220, v60, v132
	v_fmac_f32_e32 v221, v60, v133
	v_fmac_f32_e32 v222, v60, v134
	v_fmac_f32_e32 v223, v60, v135
	v_fmac_f32_e32 v224, v64, v132
	v_fmac_f32_e32 v225, v64, v133
	v_fmac_f32_e32 v226, v64, v134
	v_fmac_f32_e32 v227, v64, v135
	v_fmac_f32_e32 v228, v68, v132
	v_fmac_f32_e32 v229, v68, v133
	v_fmac_f32_e32 v230, v68, v134
	v_fmac_f32_e32 v231, v68, v135
	global_load_dwordx4 v[132:135], v108, s[24:25] nt
	s_add_u32 s24, s24, 0xc000
	s_addc_u32 s25, s25, 0
	s_waitcnt vmcnt(16)
	v_fmac_f32_e32 v196, v37, v136
	v_fmac_f32_e32 v197, v37, v137
	v_fmac_f32_e32 v198, v37, v138
	v_fmac_f32_e32 v199, v37, v139
	v_fmac_f32_e32 v200, v41, v136
	v_fmac_f32_e32 v201, v41, v137
	v_fmac_f32_e32 v202, v41, v138
	v_fmac_f32_e32 v203, v41, v139
	v_fmac_f32_e32 v204, v45, v136
	v_fmac_f32_e32 v205, v45, v137
	v_fmac_f32_e32 v206, v45, v138
	v_fmac_f32_e32 v207, v45, v139
	v_fmac_f32_e32 v208, v49, v136
	v_fmac_f32_e32 v209, v49, v137
	v_fmac_f32_e32 v210, v49, v138
	v_fmac_f32_e32 v211, v49, v139
	v_fmac_f32_e32 v212, v53, v136
	v_fmac_f32_e32 v213, v53, v137
	v_fmac_f32_e32 v214, v53, v138
	v_fmac_f32_e32 v215, v53, v139
	v_fmac_f32_e32 v216, v57, v136
	v_fmac_f32_e32 v217, v57, v137
	v_fmac_f32_e32 v218, v57, v138
	v_fmac_f32_e32 v219, v57, v139
	v_fmac_f32_e32 v220, v61, v136
	v_fmac_f32_e32 v221, v61, v137
	v_fmac_f32_e32 v222, v61, v138
	v_fmac_f32_e32 v223, v61, v139
	v_fmac_f32_e32 v224, v65, v136
	v_fmac_f32_e32 v225, v65, v137
	v_fmac_f32_e32 v226, v65, v138
	v_fmac_f32_e32 v227, v65, v139
	v_fmac_f32_e32 v228, v69, v136
	v_fmac_f32_e32 v229, v69, v137
	v_fmac_f32_e32 v230, v69, v138
	v_fmac_f32_e32 v231, v69, v139
	global_load_dwordx4 v[136:139], v108, s[24:25] nt
	s_add_u32 s24, s24, 0xc000
	s_addc_u32 s25, s25, 0
	s_waitcnt vmcnt(16)
	v_fmac_f32_e32 v196, v38, v140
	v_fmac_f32_e32 v197, v38, v141
	v_fmac_f32_e32 v198, v38, v142
	v_fmac_f32_e32 v199, v38, v143
	v_fmac_f32_e32 v200, v42, v140
	v_fmac_f32_e32 v201, v42, v141
	v_fmac_f32_e32 v202, v42, v142
	v_fmac_f32_e32 v203, v42, v143
	v_fmac_f32_e32 v204, v46, v140
	v_fmac_f32_e32 v205, v46, v141
	v_fmac_f32_e32 v206, v46, v142
	v_fmac_f32_e32 v207, v46, v143
	v_fmac_f32_e32 v208, v50, v140
	v_fmac_f32_e32 v209, v50, v141
	v_fmac_f32_e32 v210, v50, v142
	v_fmac_f32_e32 v211, v50, v143
	v_fmac_f32_e32 v212, v54, v140
	v_fmac_f32_e32 v213, v54, v141
	v_fmac_f32_e32 v214, v54, v142
	v_fmac_f32_e32 v215, v54, v143
	v_fmac_f32_e32 v216, v58, v140
	v_fmac_f32_e32 v217, v58, v141
	v_fmac_f32_e32 v218, v58, v142
	v_fmac_f32_e32 v219, v58, v143
	v_fmac_f32_e32 v220, v62, v140
	v_fmac_f32_e32 v221, v62, v141
	v_fmac_f32_e32 v222, v62, v142
	v_fmac_f32_e32 v223, v62, v143
	v_fmac_f32_e32 v224, v66, v140
	v_fmac_f32_e32 v225, v66, v141
	v_fmac_f32_e32 v226, v66, v142
	v_fmac_f32_e32 v227, v66, v143
	v_fmac_f32_e32 v228, v70, v140
	v_fmac_f32_e32 v229, v70, v141
	v_fmac_f32_e32 v230, v70, v142
	v_fmac_f32_e32 v231, v70, v143
	global_load_dwordx4 v[140:143], v108, s[24:25] nt
	s_add_u32 s24, s24, 0xc000
	s_addc_u32 s25, s25, 0
	s_waitcnt vmcnt(16)
	v_fmac_f32_e32 v196, v39, v144
	v_fmac_f32_e32 v197, v39, v145
	v_fmac_f32_e32 v198, v39, v146
	v_fmac_f32_e32 v199, v39, v147
	v_fmac_f32_e32 v200, v43, v144
	v_fmac_f32_e32 v201, v43, v145
	v_fmac_f32_e32 v202, v43, v146
	v_fmac_f32_e32 v203, v43, v147
	v_fmac_f32_e32 v204, v47, v144
	v_fmac_f32_e32 v205, v47, v145
	v_fmac_f32_e32 v206, v47, v146
	v_fmac_f32_e32 v207, v47, v147
	v_fmac_f32_e32 v208, v51, v144
	v_fmac_f32_e32 v209, v51, v145
	v_fmac_f32_e32 v210, v51, v146
	v_fmac_f32_e32 v211, v51, v147
	v_fmac_f32_e32 v212, v55, v144
	v_fmac_f32_e32 v213, v55, v145
	v_fmac_f32_e32 v214, v55, v146
	v_fmac_f32_e32 v215, v55, v147
	v_fmac_f32_e32 v216, v59, v144
	v_fmac_f32_e32 v217, v59, v145
	v_fmac_f32_e32 v218, v59, v146
	v_fmac_f32_e32 v219, v59, v147
	v_fmac_f32_e32 v220, v63, v144
	v_fmac_f32_e32 v221, v63, v145
	v_fmac_f32_e32 v222, v63, v146
	v_fmac_f32_e32 v223, v63, v147
	v_fmac_f32_e32 v224, v67, v144
	v_fmac_f32_e32 v225, v67, v145
	v_fmac_f32_e32 v226, v67, v146
	v_fmac_f32_e32 v227, v67, v147
	v_fmac_f32_e32 v228, v71, v144
	v_fmac_f32_e32 v229, v71, v145
	v_fmac_f32_e32 v230, v71, v146
	v_fmac_f32_e32 v231, v71, v147
	global_load_dwordx4 v[144:147], v108, s[24:25] nt
	s_add_u32 s24, s24, 0xc000
	s_addc_u32 s25, s25, 0
	ds_read_b128 v[36:39], v109 offset:32
	ds_read_b128 v[40:43], v109 offset:8224
	ds_read_b128 v[44:47], v109 offset:16416
	ds_read_b128 v[48:51], v109 offset:24608
	ds_read_b128 v[52:55], v109 offset:32800
	ds_read_b128 v[56:59], v109 offset:40992
	ds_read_b128 v[60:63], v109 offset:49184
	ds_read_b128 v[64:67], v109 offset:57376
	ds_read_b128 v[68:71], v110 offset:32
	s_waitcnt lgkmcnt(9)
	s_waitcnt vmcnt(16)
	v_fmac_f32_e32 v196, v72, v148
	v_fmac_f32_e32 v197, v72, v149
	v_fmac_f32_e32 v198, v72, v150
	v_fmac_f32_e32 v199, v72, v151
	v_fmac_f32_e32 v200, v76, v148
	v_fmac_f32_e32 v201, v76, v149
	v_fmac_f32_e32 v202, v76, v150
	v_fmac_f32_e32 v203, v76, v151
	v_fmac_f32_e32 v204, v80, v148
	v_fmac_f32_e32 v205, v80, v149
	v_fmac_f32_e32 v206, v80, v150
	v_fmac_f32_e32 v207, v80, v151
	v_fmac_f32_e32 v208, v84, v148
	v_fmac_f32_e32 v209, v84, v149
	v_fmac_f32_e32 v210, v84, v150
	v_fmac_f32_e32 v211, v84, v151
	v_fmac_f32_e32 v212, v88, v148
	v_fmac_f32_e32 v213, v88, v149
	v_fmac_f32_e32 v214, v88, v150
	v_fmac_f32_e32 v215, v88, v151
	v_fmac_f32_e32 v216, v92, v148
	v_fmac_f32_e32 v217, v92, v149
	v_fmac_f32_e32 v218, v92, v150
	v_fmac_f32_e32 v219, v92, v151
	v_fmac_f32_e32 v220, v96, v148
	v_fmac_f32_e32 v221, v96, v149
	v_fmac_f32_e32 v222, v96, v150
	v_fmac_f32_e32 v223, v96, v151
	v_fmac_f32_e32 v224, v100, v148
	v_fmac_f32_e32 v225, v100, v149
	v_fmac_f32_e32 v226, v100, v150
	v_fmac_f32_e32 v227, v100, v151
	v_fmac_f32_e32 v228, v104, v148
	v_fmac_f32_e32 v229, v104, v149
	v_fmac_f32_e32 v230, v104, v150
	v_fmac_f32_e32 v231, v104, v151
	global_load_dwordx4 v[148:151], v108, s[24:25] nt
	s_add_u32 s24, s24, 0xc000
	s_addc_u32 s25, s25, 0
	s_waitcnt vmcnt(16)
	v_fmac_f32_e32 v196, v73, v152
	v_fmac_f32_e32 v197, v73, v153
	v_fmac_f32_e32 v198, v73, v154
	v_fmac_f32_e32 v199, v73, v155
	v_fmac_f32_e32 v200, v77, v152
	v_fmac_f32_e32 v201, v77, v153
	v_fmac_f32_e32 v202, v77, v154
	v_fmac_f32_e32 v203, v77, v155
	v_fmac_f32_e32 v204, v81, v152
	v_fmac_f32_e32 v205, v81, v153
	v_fmac_f32_e32 v206, v81, v154
	v_fmac_f32_e32 v207, v81, v155
	v_fmac_f32_e32 v208, v85, v152
	v_fmac_f32_e32 v209, v85, v153
	v_fmac_f32_e32 v210, v85, v154
	v_fmac_f32_e32 v211, v85, v155
	v_fmac_f32_e32 v212, v89, v152
	v_fmac_f32_e32 v213, v89, v153
	v_fmac_f32_e32 v214, v89, v154
	v_fmac_f32_e32 v215, v89, v155
	v_fmac_f32_e32 v216, v93, v152
	v_fmac_f32_e32 v217, v93, v153
	v_fmac_f32_e32 v218, v93, v154
	v_fmac_f32_e32 v219, v93, v155
	v_fmac_f32_e32 v220, v97, v152
	v_fmac_f32_e32 v221, v97, v153
	v_fmac_f32_e32 v222, v97, v154
	v_fmac_f32_e32 v223, v97, v155
	v_fmac_f32_e32 v224, v101, v152
	v_fmac_f32_e32 v225, v101, v153
	v_fmac_f32_e32 v226, v101, v154
	v_fmac_f32_e32 v227, v101, v155
	v_fmac_f32_e32 v228, v105, v152
	v_fmac_f32_e32 v229, v105, v153
	v_fmac_f32_e32 v230, v105, v154
	v_fmac_f32_e32 v231, v105, v155
	global_load_dwordx4 v[152:155], v108, s[24:25] nt
	s_add_u32 s24, s24, 0xc000
	s_addc_u32 s25, s25, 0
	s_waitcnt vmcnt(16)
	v_fmac_f32_e32 v196, v74, v156
	v_fmac_f32_e32 v197, v74, v157
	v_fmac_f32_e32 v198, v74, v158
	v_fmac_f32_e32 v199, v74, v159
	v_fmac_f32_e32 v200, v78, v156
	v_fmac_f32_e32 v201, v78, v157
	v_fmac_f32_e32 v202, v78, v158
	v_fmac_f32_e32 v203, v78, v159
	v_fmac_f32_e32 v204, v82, v156
	v_fmac_f32_e32 v205, v82, v157
	v_fmac_f32_e32 v206, v82, v158
	v_fmac_f32_e32 v207, v82, v159
	v_fmac_f32_e32 v208, v86, v156
	v_fmac_f32_e32 v209, v86, v157
	v_fmac_f32_e32 v210, v86, v158
	v_fmac_f32_e32 v211, v86, v159
	v_fmac_f32_e32 v212, v90, v156
	v_fmac_f32_e32 v213, v90, v157
	v_fmac_f32_e32 v214, v90, v158
	v_fmac_f32_e32 v215, v90, v159
	v_fmac_f32_e32 v216, v94, v156
	v_fmac_f32_e32 v217, v94, v157
	v_fmac_f32_e32 v218, v94, v158
	v_fmac_f32_e32 v219, v94, v159
	v_fmac_f32_e32 v220, v98, v156
	v_fmac_f32_e32 v221, v98, v157
	v_fmac_f32_e32 v222, v98, v158
	v_fmac_f32_e32 v223, v98, v159
	v_fmac_f32_e32 v224, v102, v156
	v_fmac_f32_e32 v225, v102, v157
	v_fmac_f32_e32 v226, v102, v158
	v_fmac_f32_e32 v227, v102, v159
	v_fmac_f32_e32 v228, v106, v156
	v_fmac_f32_e32 v229, v106, v157
	v_fmac_f32_e32 v230, v106, v158
	v_fmac_f32_e32 v231, v106, v159
	global_load_dwordx4 v[156:159], v108, s[24:25] nt
	s_add_u32 s24, s24, 0xc000
	s_addc_u32 s25, s25, 0
	s_waitcnt vmcnt(16)
	v_fmac_f32_e32 v196, v75, v160
	v_fmac_f32_e32 v197, v75, v161
	v_fmac_f32_e32 v198, v75, v162
	v_fmac_f32_e32 v199, v75, v163
	v_fmac_f32_e32 v200, v79, v160
	v_fmac_f32_e32 v201, v79, v161
	v_fmac_f32_e32 v202, v79, v162
	v_fmac_f32_e32 v203, v79, v163
	v_fmac_f32_e32 v204, v83, v160
	v_fmac_f32_e32 v205, v83, v161
	v_fmac_f32_e32 v206, v83, v162
	v_fmac_f32_e32 v207, v83, v163
	v_fmac_f32_e32 v208, v87, v160
	v_fmac_f32_e32 v209, v87, v161
	v_fmac_f32_e32 v210, v87, v162
	v_fmac_f32_e32 v211, v87, v163
	v_fmac_f32_e32 v212, v91, v160
	v_fmac_f32_e32 v213, v91, v161
	v_fmac_f32_e32 v214, v91, v162
	v_fmac_f32_e32 v215, v91, v163
	v_fmac_f32_e32 v216, v95, v160
	v_fmac_f32_e32 v217, v95, v161
	v_fmac_f32_e32 v218, v95, v162
	v_fmac_f32_e32 v219, v95, v163
	v_fmac_f32_e32 v220, v99, v160
	v_fmac_f32_e32 v221, v99, v161
	v_fmac_f32_e32 v222, v99, v162
	v_fmac_f32_e32 v223, v99, v163
	v_fmac_f32_e32 v224, v103, v160
	v_fmac_f32_e32 v225, v103, v161
	v_fmac_f32_e32 v226, v103, v162
	v_fmac_f32_e32 v227, v103, v163
	v_fmac_f32_e32 v228, v107, v160
	v_fmac_f32_e32 v229, v107, v161
	v_fmac_f32_e32 v230, v107, v162
	v_fmac_f32_e32 v231, v107, v163
	global_load_dwordx4 v[160:163], v108, s[24:25] nt
	s_add_u32 s24, s24, 0xc000
	s_addc_u32 s25, s25, 0
	ds_read_b128 v[72:75], v109 offset:48
	ds_read_b128 v[76:79], v109 offset:8240
	ds_read_b128 v[80:83], v109 offset:16432
	ds_read_b128 v[84:87], v109 offset:24624
	ds_read_b128 v[88:91], v109 offset:32816
	ds_read_b128 v[92:95], v109 offset:41008
	ds_read_b128 v[96:99], v109 offset:49200
	ds_read_b128 v[100:103], v109 offset:57392
	ds_read_b128 v[104:107], v110 offset:48
	s_waitcnt lgkmcnt(9)
	s_waitcnt vmcnt(16)
	v_fmac_f32_e32 v196, v36, v164
	v_fmac_f32_e32 v197, v36, v165
	v_fmac_f32_e32 v198, v36, v166
	v_fmac_f32_e32 v199, v36, v167
	v_fmac_f32_e32 v200, v40, v164
	v_fmac_f32_e32 v201, v40, v165
	v_fmac_f32_e32 v202, v40, v166
	v_fmac_f32_e32 v203, v40, v167
	v_fmac_f32_e32 v204, v44, v164
	v_fmac_f32_e32 v205, v44, v165
	v_fmac_f32_e32 v206, v44, v166
	v_fmac_f32_e32 v207, v44, v167
	v_fmac_f32_e32 v208, v48, v164
	v_fmac_f32_e32 v209, v48, v165
	v_fmac_f32_e32 v210, v48, v166
	v_fmac_f32_e32 v211, v48, v167
	v_fmac_f32_e32 v212, v52, v164
	v_fmac_f32_e32 v213, v52, v165
	v_fmac_f32_e32 v214, v52, v166
	v_fmac_f32_e32 v215, v52, v167
	v_fmac_f32_e32 v216, v56, v164
	v_fmac_f32_e32 v217, v56, v165
	v_fmac_f32_e32 v218, v56, v166
	v_fmac_f32_e32 v219, v56, v167
	v_fmac_f32_e32 v220, v60, v164
	v_fmac_f32_e32 v221, v60, v165
	v_fmac_f32_e32 v222, v60, v166
	v_fmac_f32_e32 v223, v60, v167
	v_fmac_f32_e32 v224, v64, v164
	v_fmac_f32_e32 v225, v64, v165
	v_fmac_f32_e32 v226, v64, v166
	v_fmac_f32_e32 v227, v64, v167
	v_fmac_f32_e32 v228, v68, v164
	v_fmac_f32_e32 v229, v68, v165
	v_fmac_f32_e32 v230, v68, v166
	v_fmac_f32_e32 v231, v68, v167
	global_load_dwordx4 v[164:167], v108, s[24:25] nt
	s_add_u32 s24, s24, 0xc000
	s_addc_u32 s25, s25, 0
	s_waitcnt vmcnt(16)
	v_fmac_f32_e32 v196, v37, v168
	v_fmac_f32_e32 v197, v37, v169
	v_fmac_f32_e32 v198, v37, v170
	v_fmac_f32_e32 v199, v37, v171
	v_fmac_f32_e32 v200, v41, v168
	v_fmac_f32_e32 v201, v41, v169
	v_fmac_f32_e32 v202, v41, v170
	v_fmac_f32_e32 v203, v41, v171
	v_fmac_f32_e32 v204, v45, v168
	v_fmac_f32_e32 v205, v45, v169
	v_fmac_f32_e32 v206, v45, v170
	v_fmac_f32_e32 v207, v45, v171
	v_fmac_f32_e32 v208, v49, v168
	v_fmac_f32_e32 v209, v49, v169
	v_fmac_f32_e32 v210, v49, v170
	v_fmac_f32_e32 v211, v49, v171
	v_fmac_f32_e32 v212, v53, v168
	v_fmac_f32_e32 v213, v53, v169
	v_fmac_f32_e32 v214, v53, v170
	v_fmac_f32_e32 v215, v53, v171
	v_fmac_f32_e32 v216, v57, v168
	v_fmac_f32_e32 v217, v57, v169
	v_fmac_f32_e32 v218, v57, v170
	v_fmac_f32_e32 v219, v57, v171
	v_fmac_f32_e32 v220, v61, v168
	v_fmac_f32_e32 v221, v61, v169
	v_fmac_f32_e32 v222, v61, v170
	v_fmac_f32_e32 v223, v61, v171
	v_fmac_f32_e32 v224, v65, v168
	v_fmac_f32_e32 v225, v65, v169
	v_fmac_f32_e32 v226, v65, v170
	v_fmac_f32_e32 v227, v65, v171
	v_fmac_f32_e32 v228, v69, v168
	v_fmac_f32_e32 v229, v69, v169
	v_fmac_f32_e32 v230, v69, v170
	v_fmac_f32_e32 v231, v69, v171
	global_load_dwordx4 v[168:171], v108, s[24:25] nt
	s_add_u32 s24, s24, 0xc000
	s_addc_u32 s25, s25, 0
	s_waitcnt vmcnt(16)
	v_fmac_f32_e32 v196, v38, v172
	v_fmac_f32_e32 v197, v38, v173
	v_fmac_f32_e32 v198, v38, v174
	v_fmac_f32_e32 v199, v38, v175
	v_fmac_f32_e32 v200, v42, v172
	v_fmac_f32_e32 v201, v42, v173
	v_fmac_f32_e32 v202, v42, v174
	v_fmac_f32_e32 v203, v42, v175
	v_fmac_f32_e32 v204, v46, v172
	v_fmac_f32_e32 v205, v46, v173
	v_fmac_f32_e32 v206, v46, v174
	v_fmac_f32_e32 v207, v46, v175
	v_fmac_f32_e32 v208, v50, v172
	v_fmac_f32_e32 v209, v50, v173
	v_fmac_f32_e32 v210, v50, v174
	v_fmac_f32_e32 v211, v50, v175
	v_fmac_f32_e32 v212, v54, v172
	v_fmac_f32_e32 v213, v54, v173
	v_fmac_f32_e32 v214, v54, v174
	v_fmac_f32_e32 v215, v54, v175
	v_fmac_f32_e32 v216, v58, v172
	v_fmac_f32_e32 v217, v58, v173
	v_fmac_f32_e32 v218, v58, v174
	v_fmac_f32_e32 v219, v58, v175
	v_fmac_f32_e32 v220, v62, v172
	v_fmac_f32_e32 v221, v62, v173
	v_fmac_f32_e32 v222, v62, v174
	v_fmac_f32_e32 v223, v62, v175
	v_fmac_f32_e32 v224, v66, v172
	v_fmac_f32_e32 v225, v66, v173
	v_fmac_f32_e32 v226, v66, v174
	v_fmac_f32_e32 v227, v66, v175
	v_fmac_f32_e32 v228, v70, v172
	v_fmac_f32_e32 v229, v70, v173
	v_fmac_f32_e32 v230, v70, v174
	v_fmac_f32_e32 v231, v70, v175
	global_load_dwordx4 v[172:175], v108, s[24:25] nt
	s_add_u32 s24, s24, 0xc000
	s_addc_u32 s25, s25, 0
	s_waitcnt vmcnt(16)
	v_fmac_f32_e32 v196, v39, v176
	v_fmac_f32_e32 v197, v39, v177
	v_fmac_f32_e32 v198, v39, v178
	v_fmac_f32_e32 v199, v39, v179
	v_fmac_f32_e32 v200, v43, v176
	v_fmac_f32_e32 v201, v43, v177
	v_fmac_f32_e32 v202, v43, v178
	v_fmac_f32_e32 v203, v43, v179
	v_fmac_f32_e32 v204, v47, v176
	v_fmac_f32_e32 v205, v47, v177
	v_fmac_f32_e32 v206, v47, v178
	v_fmac_f32_e32 v207, v47, v179
	v_fmac_f32_e32 v208, v51, v176
	v_fmac_f32_e32 v209, v51, v177
	v_fmac_f32_e32 v210, v51, v178
	v_fmac_f32_e32 v211, v51, v179
	v_fmac_f32_e32 v212, v55, v176
	v_fmac_f32_e32 v213, v55, v177
	v_fmac_f32_e32 v214, v55, v178
	v_fmac_f32_e32 v215, v55, v179
	v_fmac_f32_e32 v216, v59, v176
	v_fmac_f32_e32 v217, v59, v177
	v_fmac_f32_e32 v218, v59, v178
	v_fmac_f32_e32 v219, v59, v179
	v_fmac_f32_e32 v220, v63, v176
	v_fmac_f32_e32 v221, v63, v177
	v_fmac_f32_e32 v222, v63, v178
	v_fmac_f32_e32 v223, v63, v179
	v_fmac_f32_e32 v224, v67, v176
	v_fmac_f32_e32 v225, v67, v177
	v_fmac_f32_e32 v226, v67, v178
	v_fmac_f32_e32 v227, v67, v179
	v_fmac_f32_e32 v228, v71, v176
	v_fmac_f32_e32 v229, v71, v177
	v_fmac_f32_e32 v230, v71, v178
	v_fmac_f32_e32 v231, v71, v179
	global_load_dwordx4 v[176:179], v108, s[24:25] nt
	s_add_u32 s24, s24, 0xc000
	s_addc_u32 s25, s25, 0
	ds_read_b128 v[36:39], v109 offset:64
	ds_read_b128 v[40:43], v109 offset:8256
	ds_read_b128 v[44:47], v109 offset:16448
	ds_read_b128 v[48:51], v109 offset:24640
	ds_read_b128 v[52:55], v109 offset:32832
	ds_read_b128 v[56:59], v109 offset:41024
	ds_read_b128 v[60:63], v109 offset:49216
	ds_read_b128 v[64:67], v109 offset:57408
	ds_read_b128 v[68:71], v110 offset:64
	s_waitcnt lgkmcnt(9)
	s_waitcnt vmcnt(16)
	v_fmac_f32_e32 v196, v72, v180
	v_fmac_f32_e32 v197, v72, v181
	v_fmac_f32_e32 v198, v72, v182
	v_fmac_f32_e32 v199, v72, v183
	v_fmac_f32_e32 v200, v76, v180
	v_fmac_f32_e32 v201, v76, v181
	v_fmac_f32_e32 v202, v76, v182
	v_fmac_f32_e32 v203, v76, v183
	v_fmac_f32_e32 v204, v80, v180
	v_fmac_f32_e32 v205, v80, v181
	v_fmac_f32_e32 v206, v80, v182
	v_fmac_f32_e32 v207, v80, v183
	v_fmac_f32_e32 v208, v84, v180
	v_fmac_f32_e32 v209, v84, v181
	v_fmac_f32_e32 v210, v84, v182
	v_fmac_f32_e32 v211, v84, v183
	v_fmac_f32_e32 v212, v88, v180
	v_fmac_f32_e32 v213, v88, v181
	v_fmac_f32_e32 v214, v88, v182
	v_fmac_f32_e32 v215, v88, v183
	v_fmac_f32_e32 v216, v92, v180
	v_fmac_f32_e32 v217, v92, v181
	v_fmac_f32_e32 v218, v92, v182
	v_fmac_f32_e32 v219, v92, v183
	v_fmac_f32_e32 v220, v96, v180
	v_fmac_f32_e32 v221, v96, v181
	v_fmac_f32_e32 v222, v96, v182
	v_fmac_f32_e32 v223, v96, v183
	v_fmac_f32_e32 v224, v100, v180
	v_fmac_f32_e32 v225, v100, v181
	v_fmac_f32_e32 v226, v100, v182
	v_fmac_f32_e32 v227, v100, v183
	v_fmac_f32_e32 v228, v104, v180
	v_fmac_f32_e32 v229, v104, v181
	v_fmac_f32_e32 v230, v104, v182
	v_fmac_f32_e32 v231, v104, v183
	global_load_dwordx4 v[180:183], v108, s[24:25] nt
	s_add_u32 s24, s24, 0xc000
	s_addc_u32 s25, s25, 0
	s_waitcnt vmcnt(16)
	v_fmac_f32_e32 v196, v73, v184
	v_fmac_f32_e32 v197, v73, v185
	v_fmac_f32_e32 v198, v73, v186
	v_fmac_f32_e32 v199, v73, v187
	v_fmac_f32_e32 v200, v77, v184
	v_fmac_f32_e32 v201, v77, v185
	v_fmac_f32_e32 v202, v77, v186
	v_fmac_f32_e32 v203, v77, v187
	v_fmac_f32_e32 v204, v81, v184
	v_fmac_f32_e32 v205, v81, v185
	v_fmac_f32_e32 v206, v81, v186
	v_fmac_f32_e32 v207, v81, v187
	v_fmac_f32_e32 v208, v85, v184
	v_fmac_f32_e32 v209, v85, v185
	v_fmac_f32_e32 v210, v85, v186
	v_fmac_f32_e32 v211, v85, v187
	v_fmac_f32_e32 v212, v89, v184
	v_fmac_f32_e32 v213, v89, v185
	v_fmac_f32_e32 v214, v89, v186
	v_fmac_f32_e32 v215, v89, v187
	v_fmac_f32_e32 v216, v93, v184
	v_fmac_f32_e32 v217, v93, v185
	v_fmac_f32_e32 v218, v93, v186
	v_fmac_f32_e32 v219, v93, v187
	v_fmac_f32_e32 v220, v97, v184
	v_fmac_f32_e32 v221, v97, v185
	v_fmac_f32_e32 v222, v97, v186
	v_fmac_f32_e32 v223, v97, v187
	v_fmac_f32_e32 v224, v101, v184
	v_fmac_f32_e32 v225, v101, v185
	v_fmac_f32_e32 v226, v101, v186
	v_fmac_f32_e32 v227, v101, v187
	v_fmac_f32_e32 v228, v105, v184
	v_fmac_f32_e32 v229, v105, v185
	v_fmac_f32_e32 v230, v105, v186
	v_fmac_f32_e32 v231, v105, v187
	global_load_dwordx4 v[184:187], v108, s[24:25] nt
	s_add_u32 s24, s24, 0xc000
	s_addc_u32 s25, s25, 0
	s_waitcnt vmcnt(16)
	v_fmac_f32_e32 v196, v74, v188
	v_fmac_f32_e32 v197, v74, v189
	v_fmac_f32_e32 v198, v74, v190
	v_fmac_f32_e32 v199, v74, v191
	v_fmac_f32_e32 v200, v78, v188
	v_fmac_f32_e32 v201, v78, v189
	v_fmac_f32_e32 v202, v78, v190
	v_fmac_f32_e32 v203, v78, v191
	v_fmac_f32_e32 v204, v82, v188
	v_fmac_f32_e32 v205, v82, v189
	v_fmac_f32_e32 v206, v82, v190
	v_fmac_f32_e32 v207, v82, v191
	v_fmac_f32_e32 v208, v86, v188
	v_fmac_f32_e32 v209, v86, v189
	v_fmac_f32_e32 v210, v86, v190
	v_fmac_f32_e32 v211, v86, v191
	v_fmac_f32_e32 v212, v90, v188
	v_fmac_f32_e32 v213, v90, v189
	v_fmac_f32_e32 v214, v90, v190
	v_fmac_f32_e32 v215, v90, v191
	v_fmac_f32_e32 v216, v94, v188
	v_fmac_f32_e32 v217, v94, v189
	v_fmac_f32_e32 v218, v94, v190
	v_fmac_f32_e32 v219, v94, v191
	v_fmac_f32_e32 v220, v98, v188
	v_fmac_f32_e32 v221, v98, v189
	v_fmac_f32_e32 v222, v98, v190
	v_fmac_f32_e32 v223, v98, v191
	v_fmac_f32_e32 v224, v102, v188
	v_fmac_f32_e32 v225, v102, v189
	v_fmac_f32_e32 v226, v102, v190
	v_fmac_f32_e32 v227, v102, v191
	v_fmac_f32_e32 v228, v106, v188
	v_fmac_f32_e32 v229, v106, v189
	v_fmac_f32_e32 v230, v106, v190
	v_fmac_f32_e32 v231, v106, v191
	global_load_dwordx4 v[188:191], v108, s[24:25] nt
	s_add_u32 s24, s24, 0xc000
	s_addc_u32 s25, s25, 0
	s_waitcnt vmcnt(16)
	v_fmac_f32_e32 v196, v75, v192
	v_fmac_f32_e32 v197, v75, v193
	v_fmac_f32_e32 v198, v75, v194
	v_fmac_f32_e32 v199, v75, v195
	v_fmac_f32_e32 v200, v79, v192
	v_fmac_f32_e32 v201, v79, v193
	v_fmac_f32_e32 v202, v79, v194
	v_fmac_f32_e32 v203, v79, v195
	v_fmac_f32_e32 v204, v83, v192
	v_fmac_f32_e32 v205, v83, v193
	v_fmac_f32_e32 v206, v83, v194
	v_fmac_f32_e32 v207, v83, v195
	v_fmac_f32_e32 v208, v87, v192
	v_fmac_f32_e32 v209, v87, v193
	v_fmac_f32_e32 v210, v87, v194
	v_fmac_f32_e32 v211, v87, v195
	v_fmac_f32_e32 v212, v91, v192
	v_fmac_f32_e32 v213, v91, v193
	v_fmac_f32_e32 v214, v91, v194
	v_fmac_f32_e32 v215, v91, v195
	v_fmac_f32_e32 v216, v95, v192
	v_fmac_f32_e32 v217, v95, v193
	v_fmac_f32_e32 v218, v95, v194
	v_fmac_f32_e32 v219, v95, v195
	v_fmac_f32_e32 v220, v99, v192
	v_fmac_f32_e32 v221, v99, v193
	v_fmac_f32_e32 v222, v99, v194
	v_fmac_f32_e32 v223, v99, v195
	v_fmac_f32_e32 v224, v103, v192
	v_fmac_f32_e32 v225, v103, v193
	v_fmac_f32_e32 v226, v103, v194
	v_fmac_f32_e32 v227, v103, v195
	v_fmac_f32_e32 v228, v107, v192
	v_fmac_f32_e32 v229, v107, v193
	v_fmac_f32_e32 v230, v107, v194
	v_fmac_f32_e32 v231, v107, v195
	global_load_dwordx4 v[192:195], v108, s[24:25] nt
	s_add_u32 s24, s24, 0xc000
	s_addc_u32 s25, s25, 0
	ds_read_b128 v[72:75], v109 offset:80
	ds_read_b128 v[76:79], v109 offset:8272
	ds_read_b128 v[80:83], v109 offset:16464
	ds_read_b128 v[84:87], v109 offset:24656
	ds_read_b128 v[88:91], v109 offset:32848
	ds_read_b128 v[92:95], v109 offset:41040
	ds_read_b128 v[96:99], v109 offset:49232
	ds_read_b128 v[100:103], v109 offset:57424
	ds_read_b128 v[104:107], v110 offset:80
	s_waitcnt lgkmcnt(9)
	s_waitcnt vmcnt(15)
	v_fmac_f32_e32 v196, v36, v132
	v_fmac_f32_e32 v197, v36, v133
	v_fmac_f32_e32 v198, v36, v134
	v_fmac_f32_e32 v199, v36, v135
	v_fmac_f32_e32 v200, v40, v132
	v_fmac_f32_e32 v201, v40, v133
	v_fmac_f32_e32 v202, v40, v134
	v_fmac_f32_e32 v203, v40, v135
	v_fmac_f32_e32 v204, v44, v132
	v_fmac_f32_e32 v205, v44, v133
	v_fmac_f32_e32 v206, v44, v134
	v_fmac_f32_e32 v207, v44, v135
	v_fmac_f32_e32 v208, v48, v132
	v_fmac_f32_e32 v209, v48, v133
	v_fmac_f32_e32 v210, v48, v134
	v_fmac_f32_e32 v211, v48, v135
	v_fmac_f32_e32 v212, v52, v132
	v_fmac_f32_e32 v213, v52, v133
	v_fmac_f32_e32 v214, v52, v134
	v_fmac_f32_e32 v215, v52, v135
	v_fmac_f32_e32 v216, v56, v132
	v_fmac_f32_e32 v217, v56, v133
	v_fmac_f32_e32 v218, v56, v134
	v_fmac_f32_e32 v219, v56, v135
	v_fmac_f32_e32 v220, v60, v132
	v_fmac_f32_e32 v221, v60, v133
	v_fmac_f32_e32 v222, v60, v134
	v_fmac_f32_e32 v223, v60, v135
	v_fmac_f32_e32 v224, v64, v132
	v_fmac_f32_e32 v225, v64, v133
	v_fmac_f32_e32 v226, v64, v134
	v_fmac_f32_e32 v227, v64, v135
	v_fmac_f32_e32 v228, v68, v132
	v_fmac_f32_e32 v229, v68, v133
	v_fmac_f32_e32 v230, v68, v134
	v_fmac_f32_e32 v231, v68, v135
	s_mov_b64 s[24:25], s[26:27]
	global_load_dwordx4 v[132:135], v108, s[24:25] nt
	s_add_u32 s24, s24, 0xc000
	s_addc_u32 s25, s25, 0
	s_waitcnt vmcnt(15)
	v_fmac_f32_e32 v196, v37, v136
	v_fmac_f32_e32 v197, v37, v137
	v_fmac_f32_e32 v198, v37, v138
	v_fmac_f32_e32 v199, v37, v139
	v_fmac_f32_e32 v200, v41, v136
	v_fmac_f32_e32 v201, v41, v137
	v_fmac_f32_e32 v202, v41, v138
	v_fmac_f32_e32 v203, v41, v139
	v_fmac_f32_e32 v204, v45, v136
	v_fmac_f32_e32 v205, v45, v137
	v_fmac_f32_e32 v206, v45, v138
	v_fmac_f32_e32 v207, v45, v139
	v_fmac_f32_e32 v208, v49, v136
	v_fmac_f32_e32 v209, v49, v137
	v_fmac_f32_e32 v210, v49, v138
	v_fmac_f32_e32 v211, v49, v139
	v_fmac_f32_e32 v212, v53, v136
	v_fmac_f32_e32 v213, v53, v137
	v_fmac_f32_e32 v214, v53, v138
	v_fmac_f32_e32 v215, v53, v139
	v_fmac_f32_e32 v216, v57, v136
	v_fmac_f32_e32 v217, v57, v137
	v_fmac_f32_e32 v218, v57, v138
	v_fmac_f32_e32 v219, v57, v139
	v_fmac_f32_e32 v220, v61, v136
	v_fmac_f32_e32 v221, v61, v137
	v_fmac_f32_e32 v222, v61, v138
	v_fmac_f32_e32 v223, v61, v139
	v_fmac_f32_e32 v224, v65, v136
	v_fmac_f32_e32 v225, v65, v137
	v_fmac_f32_e32 v226, v65, v138
	v_fmac_f32_e32 v227, v65, v139
	v_fmac_f32_e32 v228, v69, v136
	v_fmac_f32_e32 v229, v69, v137
	v_fmac_f32_e32 v230, v69, v138
	v_fmac_f32_e32 v231, v69, v139
	global_load_dwordx4 v[136:139], v108, s[24:25] nt
	s_add_u32 s24, s24, 0xc000
	s_addc_u32 s25, s25, 0
	s_waitcnt vmcnt(15)
	v_fmac_f32_e32 v196, v38, v140
	v_fmac_f32_e32 v197, v38, v141
	v_fmac_f32_e32 v198, v38, v142
	v_fmac_f32_e32 v199, v38, v143
	v_fmac_f32_e32 v200, v42, v140
	v_fmac_f32_e32 v201, v42, v141
	v_fmac_f32_e32 v202, v42, v142
	v_fmac_f32_e32 v203, v42, v143
	v_fmac_f32_e32 v204, v46, v140
	v_fmac_f32_e32 v205, v46, v141
	v_fmac_f32_e32 v206, v46, v142
	v_fmac_f32_e32 v207, v46, v143
	v_fmac_f32_e32 v208, v50, v140
	v_fmac_f32_e32 v209, v50, v141
	v_fmac_f32_e32 v210, v50, v142
	v_fmac_f32_e32 v211, v50, v143
	v_fmac_f32_e32 v212, v54, v140
	v_fmac_f32_e32 v213, v54, v141
	v_fmac_f32_e32 v214, v54, v142
	v_fmac_f32_e32 v215, v54, v143
	v_fmac_f32_e32 v216, v58, v140
	v_fmac_f32_e32 v217, v58, v141
	v_fmac_f32_e32 v218, v58, v142
	v_fmac_f32_e32 v219, v58, v143
	v_fmac_f32_e32 v220, v62, v140
	v_fmac_f32_e32 v221, v62, v141
	v_fmac_f32_e32 v222, v62, v142
	v_fmac_f32_e32 v223, v62, v143
	v_fmac_f32_e32 v224, v66, v140
	v_fmac_f32_e32 v225, v66, v141
	v_fmac_f32_e32 v226, v66, v142
	v_fmac_f32_e32 v227, v66, v143
	v_fmac_f32_e32 v228, v70, v140
	v_fmac_f32_e32 v229, v70, v141
	v_fmac_f32_e32 v230, v70, v142
	v_fmac_f32_e32 v231, v70, v143
	global_load_dwordx4 v[140:143], v108, s[24:25] nt
	s_add_u32 s24, s24, 0xc000
	s_addc_u32 s25, s25, 0
	s_waitcnt vmcnt(15)
	v_fmac_f32_e32 v196, v39, v144
	v_fmac_f32_e32 v197, v39, v145
	v_fmac_f32_e32 v198, v39, v146
	v_fmac_f32_e32 v199, v39, v147
	v_fmac_f32_e32 v200, v43, v144
	v_fmac_f32_e32 v201, v43, v145
	v_fmac_f32_e32 v202, v43, v146
	v_fmac_f32_e32 v203, v43, v147
	v_fmac_f32_e32 v204, v47, v144
	v_fmac_f32_e32 v205, v47, v145
	v_fmac_f32_e32 v206, v47, v146
	v_fmac_f32_e32 v207, v47, v147
	v_fmac_f32_e32 v208, v51, v144
	v_fmac_f32_e32 v209, v51, v145
	v_fmac_f32_e32 v210, v51, v146
	v_fmac_f32_e32 v211, v51, v147
	v_fmac_f32_e32 v212, v55, v144
	v_fmac_f32_e32 v213, v55, v145
	v_fmac_f32_e32 v214, v55, v146
	v_fmac_f32_e32 v215, v55, v147
	v_fmac_f32_e32 v216, v59, v144
	v_fmac_f32_e32 v217, v59, v145
	v_fmac_f32_e32 v218, v59, v146
	v_fmac_f32_e32 v219, v59, v147
	v_fmac_f32_e32 v220, v63, v144
	v_fmac_f32_e32 v221, v63, v145
	v_fmac_f32_e32 v222, v63, v146
	v_fmac_f32_e32 v223, v63, v147
	v_fmac_f32_e32 v224, v67, v144
	v_fmac_f32_e32 v225, v67, v145
	v_fmac_f32_e32 v226, v67, v146
	v_fmac_f32_e32 v227, v67, v147
	v_fmac_f32_e32 v228, v71, v144
	v_fmac_f32_e32 v229, v71, v145
	v_fmac_f32_e32 v230, v71, v146
	v_fmac_f32_e32 v231, v71, v147
	global_load_dwordx4 v[144:147], v108, s[24:25] nt
	s_add_u32 s24, s24, 0xc000
	s_addc_u32 s25, s25, 0
	ds_read_b128 v[36:39], v109 offset:96
	ds_read_b128 v[40:43], v109 offset:8288
	ds_read_b128 v[44:47], v109 offset:16480
	ds_read_b128 v[48:51], v109 offset:24672
	ds_read_b128 v[52:55], v109 offset:32864
	ds_read_b128 v[56:59], v109 offset:41056
	ds_read_b128 v[60:63], v109 offset:49248
	ds_read_b128 v[64:67], v109 offset:57440
	ds_read_b128 v[68:71], v110 offset:96
	s_waitcnt lgkmcnt(9)
	s_waitcnt vmcnt(15)
	v_fmac_f32_e32 v196, v72, v148
	v_fmac_f32_e32 v197, v72, v149
	v_fmac_f32_e32 v198, v72, v150
	v_fmac_f32_e32 v199, v72, v151
	v_fmac_f32_e32 v200, v76, v148
	v_fmac_f32_e32 v201, v76, v149
	v_fmac_f32_e32 v202, v76, v150
	v_fmac_f32_e32 v203, v76, v151
	v_fmac_f32_e32 v204, v80, v148
	v_fmac_f32_e32 v205, v80, v149
	v_fmac_f32_e32 v206, v80, v150
	v_fmac_f32_e32 v207, v80, v151
	v_fmac_f32_e32 v208, v84, v148
	v_fmac_f32_e32 v209, v84, v149
	v_fmac_f32_e32 v210, v84, v150
	v_fmac_f32_e32 v211, v84, v151
	v_fmac_f32_e32 v212, v88, v148
	v_fmac_f32_e32 v213, v88, v149
	v_fmac_f32_e32 v214, v88, v150
	v_fmac_f32_e32 v215, v88, v151
	v_fmac_f32_e32 v216, v92, v148
	v_fmac_f32_e32 v217, v92, v149
	v_fmac_f32_e32 v218, v92, v150
	v_fmac_f32_e32 v219, v92, v151
	v_fmac_f32_e32 v220, v96, v148
	v_fmac_f32_e32 v221, v96, v149
	v_fmac_f32_e32 v222, v96, v150
	v_fmac_f32_e32 v223, v96, v151
	v_fmac_f32_e32 v224, v100, v148
	v_fmac_f32_e32 v225, v100, v149
	v_fmac_f32_e32 v226, v100, v150
	v_fmac_f32_e32 v227, v100, v151
	v_fmac_f32_e32 v228, v104, v148
	v_fmac_f32_e32 v229, v104, v149
	v_fmac_f32_e32 v230, v104, v150
	v_fmac_f32_e32 v231, v104, v151
	global_load_dwordx4 v[148:151], v108, s[24:25] nt
	s_add_u32 s24, s24, 0xc000
	s_addc_u32 s25, s25, 0
	s_waitcnt vmcnt(15)
	v_fmac_f32_e32 v196, v73, v152
	v_fmac_f32_e32 v197, v73, v153
	v_fmac_f32_e32 v198, v73, v154
	v_fmac_f32_e32 v199, v73, v155
	v_fmac_f32_e32 v200, v77, v152
	v_fmac_f32_e32 v201, v77, v153
	v_fmac_f32_e32 v202, v77, v154
	v_fmac_f32_e32 v203, v77, v155
	v_fmac_f32_e32 v204, v81, v152
	v_fmac_f32_e32 v205, v81, v153
	v_fmac_f32_e32 v206, v81, v154
	v_fmac_f32_e32 v207, v81, v155
	v_fmac_f32_e32 v208, v85, v152
	v_fmac_f32_e32 v209, v85, v153
	v_fmac_f32_e32 v210, v85, v154
	v_fmac_f32_e32 v211, v85, v155
	v_fmac_f32_e32 v212, v89, v152
	v_fmac_f32_e32 v213, v89, v153
	v_fmac_f32_e32 v214, v89, v154
	v_fmac_f32_e32 v215, v89, v155
	v_fmac_f32_e32 v216, v93, v152
	v_fmac_f32_e32 v217, v93, v153
	v_fmac_f32_e32 v218, v93, v154
	v_fmac_f32_e32 v219, v93, v155
	v_fmac_f32_e32 v220, v97, v152
	v_fmac_f32_e32 v221, v97, v153
	v_fmac_f32_e32 v222, v97, v154
	v_fmac_f32_e32 v223, v97, v155
	v_fmac_f32_e32 v224, v101, v152
	v_fmac_f32_e32 v225, v101, v153
	v_fmac_f32_e32 v226, v101, v154
	v_fmac_f32_e32 v227, v101, v155
	v_fmac_f32_e32 v228, v105, v152
	v_fmac_f32_e32 v229, v105, v153
	v_fmac_f32_e32 v230, v105, v154
	v_fmac_f32_e32 v231, v105, v155
	global_load_dwordx4 v[152:155], v108, s[24:25] nt
	s_add_u32 s24, s24, 0xc000
	s_addc_u32 s25, s25, 0
	s_waitcnt vmcnt(15)
	v_fmac_f32_e32 v196, v74, v156
	v_fmac_f32_e32 v197, v74, v157
	v_fmac_f32_e32 v198, v74, v158
	v_fmac_f32_e32 v199, v74, v159
	v_fmac_f32_e32 v200, v78, v156
	v_fmac_f32_e32 v201, v78, v157
	v_fmac_f32_e32 v202, v78, v158
	v_fmac_f32_e32 v203, v78, v159
	v_fmac_f32_e32 v204, v82, v156
	v_fmac_f32_e32 v205, v82, v157
	v_fmac_f32_e32 v206, v82, v158
	v_fmac_f32_e32 v207, v82, v159
	v_fmac_f32_e32 v208, v86, v156
	v_fmac_f32_e32 v209, v86, v157
	v_fmac_f32_e32 v210, v86, v158
	v_fmac_f32_e32 v211, v86, v159
	v_fmac_f32_e32 v212, v90, v156
	v_fmac_f32_e32 v213, v90, v157
	v_fmac_f32_e32 v214, v90, v158
	v_fmac_f32_e32 v215, v90, v159
	v_fmac_f32_e32 v216, v94, v156
	v_fmac_f32_e32 v217, v94, v157
	v_fmac_f32_e32 v218, v94, v158
	v_fmac_f32_e32 v219, v94, v159
	v_fmac_f32_e32 v220, v98, v156
	v_fmac_f32_e32 v221, v98, v157
	v_fmac_f32_e32 v222, v98, v158
	v_fmac_f32_e32 v223, v98, v159
	v_fmac_f32_e32 v224, v102, v156
	v_fmac_f32_e32 v225, v102, v157
	v_fmac_f32_e32 v226, v102, v158
	v_fmac_f32_e32 v227, v102, v159
	v_fmac_f32_e32 v228, v106, v156
	v_fmac_f32_e32 v229, v106, v157
	v_fmac_f32_e32 v230, v106, v158
	v_fmac_f32_e32 v231, v106, v159
	global_load_dwordx4 v[156:159], v108, s[24:25] nt
	s_add_u32 s24, s24, 0xc000
	s_addc_u32 s25, s25, 0
	s_waitcnt vmcnt(15)
	v_fmac_f32_e32 v196, v75, v160
	v_fmac_f32_e32 v197, v75, v161
	v_fmac_f32_e32 v198, v75, v162
	v_fmac_f32_e32 v199, v75, v163
	v_fmac_f32_e32 v200, v79, v160
	v_fmac_f32_e32 v201, v79, v161
	v_fmac_f32_e32 v202, v79, v162
	v_fmac_f32_e32 v203, v79, v163
	v_fmac_f32_e32 v204, v83, v160
	v_fmac_f32_e32 v205, v83, v161
	v_fmac_f32_e32 v206, v83, v162
	v_fmac_f32_e32 v207, v83, v163
	v_fmac_f32_e32 v208, v87, v160
	v_fmac_f32_e32 v209, v87, v161
	v_fmac_f32_e32 v210, v87, v162
	v_fmac_f32_e32 v211, v87, v163
	v_fmac_f32_e32 v212, v91, v160
	v_fmac_f32_e32 v213, v91, v161
	v_fmac_f32_e32 v214, v91, v162
	v_fmac_f32_e32 v215, v91, v163
	v_fmac_f32_e32 v216, v95, v160
	v_fmac_f32_e32 v217, v95, v161
	v_fmac_f32_e32 v218, v95, v162
	v_fmac_f32_e32 v219, v95, v163
	v_fmac_f32_e32 v220, v99, v160
	v_fmac_f32_e32 v221, v99, v161
	v_fmac_f32_e32 v222, v99, v162
	v_fmac_f32_e32 v223, v99, v163
	v_fmac_f32_e32 v224, v103, v160
	v_fmac_f32_e32 v225, v103, v161
	v_fmac_f32_e32 v226, v103, v162
	v_fmac_f32_e32 v227, v103, v163
	v_fmac_f32_e32 v228, v107, v160
	v_fmac_f32_e32 v229, v107, v161
	v_fmac_f32_e32 v230, v107, v162
	v_fmac_f32_e32 v231, v107, v163
	global_load_dwordx4 v[160:163], v108, s[24:25] nt
	s_add_u32 s24, s24, 0xc000
	s_addc_u32 s25, s25, 0
	ds_read_b128 v[72:75], v109 offset:112
	ds_read_b128 v[76:79], v109 offset:8304
	ds_read_b128 v[80:83], v109 offset:16496
	ds_read_b128 v[84:87], v109 offset:24688
	ds_read_b128 v[88:91], v109 offset:32880
	ds_read_b128 v[92:95], v109 offset:41072
	ds_read_b128 v[96:99], v109 offset:49264
	ds_read_b128 v[100:103], v109 offset:57456
	ds_read_b128 v[104:107], v110 offset:112
	s_waitcnt lgkmcnt(9)
	s_waitcnt vmcnt(15)
	v_fmac_f32_e32 v196, v36, v164
	v_fmac_f32_e32 v197, v36, v165
	v_fmac_f32_e32 v198, v36, v166
	v_fmac_f32_e32 v199, v36, v167
	v_fmac_f32_e32 v200, v40, v164
	v_fmac_f32_e32 v201, v40, v165
	v_fmac_f32_e32 v202, v40, v166
	v_fmac_f32_e32 v203, v40, v167
	v_fmac_f32_e32 v204, v44, v164
	v_fmac_f32_e32 v205, v44, v165
	v_fmac_f32_e32 v206, v44, v166
	v_fmac_f32_e32 v207, v44, v167
	v_fmac_f32_e32 v208, v48, v164
	v_fmac_f32_e32 v209, v48, v165
	v_fmac_f32_e32 v210, v48, v166
	v_fmac_f32_e32 v211, v48, v167
	v_fmac_f32_e32 v212, v52, v164
	v_fmac_f32_e32 v213, v52, v165
	v_fmac_f32_e32 v214, v52, v166
	v_fmac_f32_e32 v215, v52, v167
	v_fmac_f32_e32 v216, v56, v164
	v_fmac_f32_e32 v217, v56, v165
	v_fmac_f32_e32 v218, v56, v166
	v_fmac_f32_e32 v219, v56, v167
	v_fmac_f32_e32 v220, v60, v164
	v_fmac_f32_e32 v221, v60, v165
	v_fmac_f32_e32 v222, v60, v166
	v_fmac_f32_e32 v223, v60, v167
	v_fmac_f32_e32 v224, v64, v164
	v_fmac_f32_e32 v225, v64, v165
	v_fmac_f32_e32 v226, v64, v166
	v_fmac_f32_e32 v227, v64, v167
	v_fmac_f32_e32 v228, v68, v164
	v_fmac_f32_e32 v229, v68, v165
	v_fmac_f32_e32 v230, v68, v166
	v_fmac_f32_e32 v231, v68, v167
	global_load_dwordx4 v[164:167], v108, s[24:25] nt
	s_add_u32 s24, s24, 0xc000
	s_addc_u32 s25, s25, 0
	s_waitcnt vmcnt(15)
	v_fmac_f32_e32 v196, v37, v168
	v_fmac_f32_e32 v197, v37, v169
	v_fmac_f32_e32 v198, v37, v170
	v_fmac_f32_e32 v199, v37, v171
	v_fmac_f32_e32 v200, v41, v168
	v_fmac_f32_e32 v201, v41, v169
	v_fmac_f32_e32 v202, v41, v170
	v_fmac_f32_e32 v203, v41, v171
	v_fmac_f32_e32 v204, v45, v168
	v_fmac_f32_e32 v205, v45, v169
	v_fmac_f32_e32 v206, v45, v170
	v_fmac_f32_e32 v207, v45, v171
	v_fmac_f32_e32 v208, v49, v168
	v_fmac_f32_e32 v209, v49, v169
	v_fmac_f32_e32 v210, v49, v170
	v_fmac_f32_e32 v211, v49, v171
	v_fmac_f32_e32 v212, v53, v168
	v_fmac_f32_e32 v213, v53, v169
	v_fmac_f32_e32 v214, v53, v170
	v_fmac_f32_e32 v215, v53, v171
	v_fmac_f32_e32 v216, v57, v168
	v_fmac_f32_e32 v217, v57, v169
	v_fmac_f32_e32 v218, v57, v170
	v_fmac_f32_e32 v219, v57, v171
	v_fmac_f32_e32 v220, v61, v168
	v_fmac_f32_e32 v221, v61, v169
	v_fmac_f32_e32 v222, v61, v170
	v_fmac_f32_e32 v223, v61, v171
	v_fmac_f32_e32 v224, v65, v168
	v_fmac_f32_e32 v225, v65, v169
	v_fmac_f32_e32 v226, v65, v170
	v_fmac_f32_e32 v227, v65, v171
	v_fmac_f32_e32 v228, v69, v168
	v_fmac_f32_e32 v229, v69, v169
	v_fmac_f32_e32 v230, v69, v170
	v_fmac_f32_e32 v231, v69, v171
	global_load_dwordx4 v[168:171], v108, s[24:25] nt
	s_add_u32 s24, s24, 0xc000
	s_addc_u32 s25, s25, 0
	s_waitcnt vmcnt(15)
	v_fmac_f32_e32 v196, v38, v172
	v_fmac_f32_e32 v197, v38, v173
	v_fmac_f32_e32 v198, v38, v174
	v_fmac_f32_e32 v199, v38, v175
	v_fmac_f32_e32 v200, v42, v172
	v_fmac_f32_e32 v201, v42, v173
	v_fmac_f32_e32 v202, v42, v174
	v_fmac_f32_e32 v203, v42, v175
	v_fmac_f32_e32 v204, v46, v172
	v_fmac_f32_e32 v205, v46, v173
	v_fmac_f32_e32 v206, v46, v174
	v_fmac_f32_e32 v207, v46, v175
	v_fmac_f32_e32 v208, v50, v172
	v_fmac_f32_e32 v209, v50, v173
	v_fmac_f32_e32 v210, v50, v174
	v_fmac_f32_e32 v211, v50, v175
	v_fmac_f32_e32 v212, v54, v172
	v_fmac_f32_e32 v213, v54, v173
	v_fmac_f32_e32 v214, v54, v174
	v_fmac_f32_e32 v215, v54, v175
	v_fmac_f32_e32 v216, v58, v172
	v_fmac_f32_e32 v217, v58, v173
	v_fmac_f32_e32 v218, v58, v174
	v_fmac_f32_e32 v219, v58, v175
	v_fmac_f32_e32 v220, v62, v172
	v_fmac_f32_e32 v221, v62, v173
	v_fmac_f32_e32 v222, v62, v174
	v_fmac_f32_e32 v223, v62, v175
	v_fmac_f32_e32 v224, v66, v172
	v_fmac_f32_e32 v225, v66, v173
	v_fmac_f32_e32 v226, v66, v174
	v_fmac_f32_e32 v227, v66, v175
	v_fmac_f32_e32 v228, v70, v172
	v_fmac_f32_e32 v229, v70, v173
	v_fmac_f32_e32 v230, v70, v174
	v_fmac_f32_e32 v231, v70, v175
	global_load_dwordx4 v[172:175], v108, s[24:25] nt
	s_add_u32 s24, s24, 0xc000
	s_addc_u32 s25, s25, 0
	s_waitcnt vmcnt(15)
	v_fmac_f32_e32 v196, v39, v176
	v_fmac_f32_e32 v197, v39, v177
	v_fmac_f32_e32 v198, v39, v178
	v_fmac_f32_e32 v199, v39, v179
	v_fmac_f32_e32 v200, v43, v176
	v_fmac_f32_e32 v201, v43, v177
	v_fmac_f32_e32 v202, v43, v178
	v_fmac_f32_e32 v203, v43, v179
	v_fmac_f32_e32 v204, v47, v176
	v_fmac_f32_e32 v205, v47, v177
	v_fmac_f32_e32 v206, v47, v178
	v_fmac_f32_e32 v207, v47, v179
	v_fmac_f32_e32 v208, v51, v176
	v_fmac_f32_e32 v209, v51, v177
	v_fmac_f32_e32 v210, v51, v178
	v_fmac_f32_e32 v211, v51, v179
	v_fmac_f32_e32 v212, v55, v176
	v_fmac_f32_e32 v213, v55, v177
	v_fmac_f32_e32 v214, v55, v178
	v_fmac_f32_e32 v215, v55, v179
	v_fmac_f32_e32 v216, v59, v176
	v_fmac_f32_e32 v217, v59, v177
	v_fmac_f32_e32 v218, v59, v178
	v_fmac_f32_e32 v219, v59, v179
	v_fmac_f32_e32 v220, v63, v176
	v_fmac_f32_e32 v221, v63, v177
	v_fmac_f32_e32 v222, v63, v178
	v_fmac_f32_e32 v223, v63, v179
	v_fmac_f32_e32 v224, v67, v176
	v_fmac_f32_e32 v225, v67, v177
	v_fmac_f32_e32 v226, v67, v178
	v_fmac_f32_e32 v227, v67, v179
	v_fmac_f32_e32 v228, v71, v176
	v_fmac_f32_e32 v229, v71, v177
	v_fmac_f32_e32 v230, v71, v178
	v_fmac_f32_e32 v231, v71, v179
	global_load_dwordx4 v[176:179], v108, s[24:25] nt
	s_add_u32 s24, s24, 0xc000
	s_addc_u32 s25, s25, 0
	s_waitcnt lgkmcnt(0)
	s_waitcnt vmcnt(15)
	v_fmac_f32_e32 v196, v72, v180
	v_fmac_f32_e32 v197, v72, v181
	v_fmac_f32_e32 v198, v72, v182
	v_fmac_f32_e32 v199, v72, v183
	v_fmac_f32_e32 v200, v76, v180
	v_fmac_f32_e32 v201, v76, v181
	v_fmac_f32_e32 v202, v76, v182
	v_fmac_f32_e32 v203, v76, v183
	v_fmac_f32_e32 v204, v80, v180
	v_fmac_f32_e32 v205, v80, v181
	v_fmac_f32_e32 v206, v80, v182
	v_fmac_f32_e32 v207, v80, v183
	v_fmac_f32_e32 v208, v84, v180
	v_fmac_f32_e32 v209, v84, v181
	v_fmac_f32_e32 v210, v84, v182
	v_fmac_f32_e32 v211, v84, v183
	v_fmac_f32_e32 v212, v88, v180
	v_fmac_f32_e32 v213, v88, v181
	v_fmac_f32_e32 v214, v88, v182
	v_fmac_f32_e32 v215, v88, v183
	v_fmac_f32_e32 v216, v92, v180
	v_fmac_f32_e32 v217, v92, v181
	v_fmac_f32_e32 v218, v92, v182
	v_fmac_f32_e32 v219, v92, v183
	v_fmac_f32_e32 v220, v96, v180
	v_fmac_f32_e32 v221, v96, v181
	v_fmac_f32_e32 v222, v96, v182
	v_fmac_f32_e32 v223, v96, v183
	v_fmac_f32_e32 v224, v100, v180
	v_fmac_f32_e32 v225, v100, v181
	v_fmac_f32_e32 v226, v100, v182
	v_fmac_f32_e32 v227, v100, v183
	v_fmac_f32_e32 v228, v104, v180
	v_fmac_f32_e32 v229, v104, v181
	v_fmac_f32_e32 v230, v104, v182
	v_fmac_f32_e32 v231, v104, v183
	global_load_dwordx4 v[180:183], v108, s[24:25] nt
	s_add_u32 s24, s24, 0xc000
	s_addc_u32 s25, s25, 0
	s_waitcnt vmcnt(15)
	v_fmac_f32_e32 v196, v73, v184
	v_fmac_f32_e32 v197, v73, v185
	v_fmac_f32_e32 v198, v73, v186
	v_fmac_f32_e32 v199, v73, v187
	v_fmac_f32_e32 v200, v77, v184
	v_fmac_f32_e32 v201, v77, v185
	v_fmac_f32_e32 v202, v77, v186
	v_fmac_f32_e32 v203, v77, v187
	v_fmac_f32_e32 v204, v81, v184
	v_fmac_f32_e32 v205, v81, v185
	v_fmac_f32_e32 v206, v81, v186
	v_fmac_f32_e32 v207, v81, v187
	v_fmac_f32_e32 v208, v85, v184
	v_fmac_f32_e32 v209, v85, v185
	v_fmac_f32_e32 v210, v85, v186
	v_fmac_f32_e32 v211, v85, v187
	v_fmac_f32_e32 v212, v89, v184
	v_fmac_f32_e32 v213, v89, v185
	v_fmac_f32_e32 v214, v89, v186
	v_fmac_f32_e32 v215, v89, v187
	v_fmac_f32_e32 v216, v93, v184
	v_fmac_f32_e32 v217, v93, v185
	v_fmac_f32_e32 v218, v93, v186
	v_fmac_f32_e32 v219, v93, v187
	v_fmac_f32_e32 v220, v97, v184
	v_fmac_f32_e32 v221, v97, v185
	v_fmac_f32_e32 v222, v97, v186
	v_fmac_f32_e32 v223, v97, v187
	v_fmac_f32_e32 v224, v101, v184
	v_fmac_f32_e32 v225, v101, v185
	v_fmac_f32_e32 v226, v101, v186
	v_fmac_f32_e32 v227, v101, v187
	v_fmac_f32_e32 v228, v105, v184
	v_fmac_f32_e32 v229, v105, v185
	v_fmac_f32_e32 v230, v105, v186
	v_fmac_f32_e32 v231, v105, v187
	global_load_dwordx4 v[184:187], v108, s[24:25] nt
	s_add_u32 s24, s24, 0xc000
	s_addc_u32 s25, s25, 0
	s_waitcnt vmcnt(15)
	v_fmac_f32_e32 v196, v74, v188
	v_fmac_f32_e32 v197, v74, v189
	v_fmac_f32_e32 v198, v74, v190
	v_fmac_f32_e32 v199, v74, v191
	v_fmac_f32_e32 v200, v78, v188
	v_fmac_f32_e32 v201, v78, v189
	v_fmac_f32_e32 v202, v78, v190
	v_fmac_f32_e32 v203, v78, v191
	v_fmac_f32_e32 v204, v82, v188
	v_fmac_f32_e32 v205, v82, v189
	v_fmac_f32_e32 v206, v82, v190
	v_fmac_f32_e32 v207, v82, v191
	v_fmac_f32_e32 v208, v86, v188
	v_fmac_f32_e32 v209, v86, v189
	v_fmac_f32_e32 v210, v86, v190
	v_fmac_f32_e32 v211, v86, v191
	v_fmac_f32_e32 v212, v90, v188
	v_fmac_f32_e32 v213, v90, v189
	v_fmac_f32_e32 v214, v90, v190
	v_fmac_f32_e32 v215, v90, v191
	v_fmac_f32_e32 v216, v94, v188
	v_fmac_f32_e32 v217, v94, v189
	v_fmac_f32_e32 v218, v94, v190
	v_fmac_f32_e32 v219, v94, v191
	v_fmac_f32_e32 v220, v98, v188
	v_fmac_f32_e32 v221, v98, v189
	v_fmac_f32_e32 v222, v98, v190
	v_fmac_f32_e32 v223, v98, v191
	v_fmac_f32_e32 v224, v102, v188
	v_fmac_f32_e32 v225, v102, v189
	v_fmac_f32_e32 v226, v102, v190
	v_fmac_f32_e32 v227, v102, v191
	v_fmac_f32_e32 v228, v106, v188
	v_fmac_f32_e32 v229, v106, v189
	v_fmac_f32_e32 v230, v106, v190
	v_fmac_f32_e32 v231, v106, v191
	global_load_dwordx4 v[188:191], v108, s[24:25] nt
	s_add_u32 s24, s24, 0xc000
	s_addc_u32 s25, s25, 0
	s_waitcnt vmcnt(15)
	v_fmac_f32_e32 v196, v75, v192
	v_fmac_f32_e32 v197, v75, v193
	v_fmac_f32_e32 v198, v75, v194
	v_fmac_f32_e32 v199, v75, v195
	v_fmac_f32_e32 v200, v79, v192
	v_fmac_f32_e32 v201, v79, v193
	v_fmac_f32_e32 v202, v79, v194
	v_fmac_f32_e32 v203, v79, v195
	v_fmac_f32_e32 v204, v83, v192
	v_fmac_f32_e32 v205, v83, v193
	v_fmac_f32_e32 v206, v83, v194
	v_fmac_f32_e32 v207, v83, v195
	v_fmac_f32_e32 v208, v87, v192
	v_fmac_f32_e32 v209, v87, v193
	v_fmac_f32_e32 v210, v87, v194
	v_fmac_f32_e32 v211, v87, v195
	v_fmac_f32_e32 v212, v91, v192
	v_fmac_f32_e32 v213, v91, v193
	v_fmac_f32_e32 v214, v91, v194
	v_fmac_f32_e32 v215, v91, v195
	v_fmac_f32_e32 v216, v95, v192
	v_fmac_f32_e32 v217, v95, v193
	v_fmac_f32_e32 v218, v95, v194
	v_fmac_f32_e32 v219, v95, v195
	v_fmac_f32_e32 v220, v99, v192
	v_fmac_f32_e32 v221, v99, v193
	v_fmac_f32_e32 v222, v99, v194
	v_fmac_f32_e32 v223, v99, v195
	v_fmac_f32_e32 v224, v103, v192
	v_fmac_f32_e32 v225, v103, v193
	v_fmac_f32_e32 v226, v103, v194
	v_fmac_f32_e32 v227, v103, v195
	v_fmac_f32_e32 v228, v107, v192
	v_fmac_f32_e32 v229, v107, v193
	v_fmac_f32_e32 v230, v107, v194
	v_fmac_f32_e32 v231, v107, v195
	global_load_dwordx4 v[192:195], v108, s[24:25] nt
	s_add_u32 s24, s24, 0xc000
	s_addc_u32 s25, s25, 0
	ds_write_b128 v111, v[196:199] offset:0
	ds_write_b128 v111, v[200:203] offset:128
	ds_write_b128 v111, v[204:207] offset:256
	ds_write_b128 v111, v[208:211] offset:384
	ds_write_b128 v111, v[212:215] offset:512
	ds_write_b128 v111, v[216:219] offset:640
	ds_write_b128 v111, v[220:223] offset:768
	ds_write_b128 v111, v[224:227] offset:896
	ds_write_b128 v111, v[228:231] offset:1024
	s_waitcnt lgkmcnt(0)
	s_barrier
	v_mov_b32_e32 v117, 0
	ds_read_b32 v36, v112 offset:0
	ds_read_b32 v37, v112 offset:1152
	ds_read_b32 v38, v112 offset:2304
	ds_read_b32 v39, v112 offset:3456
	ds_read_b32 v40, v112 offset:4608
	ds_read_b32 v41, v112 offset:5760
	ds_read_b32 v42, v112 offset:6912
	ds_read_b32 v43, v112 offset:8064
	ds_read_b32 v44, v112 offset:9216
	ds_read_b32 v45, v112 offset:10368
	ds_read_b32 v46, v112 offset:11520
	ds_read_b32 v47, v112 offset:12672
	ds_read_b32 v48, v112 offset:13824
	ds_read_b32 v49, v112 offset:14976
	ds_read_b32 v50, v112 offset:16128
	ds_read_b32 v51, v112 offset:17280
	s_waitcnt lgkmcnt(15)
	v_add_f32_e32 v117, v117, v36
	s_waitcnt lgkmcnt(14)
	v_add_f32_e32 v117, v117, v37
	s_waitcnt lgkmcnt(13)
	v_add_f32_e32 v117, v117, v38
	s_waitcnt lgkmcnt(12)
	v_add_f32_e32 v117, v117, v39
	s_waitcnt lgkmcnt(11)
	v_add_f32_e32 v117, v117, v40
	s_waitcnt lgkmcnt(10)
	v_add_f32_e32 v117, v117, v41
	s_waitcnt lgkmcnt(9)
	v_add_f32_e32 v117, v117, v42
	s_waitcnt lgkmcnt(8)
	v_add_f32_e32 v117, v117, v43
	s_waitcnt lgkmcnt(7)
	v_add_f32_e32 v117, v117, v44
	s_waitcnt lgkmcnt(6)
	v_add_f32_e32 v117, v117, v45
	s_waitcnt lgkmcnt(5)
	v_add_f32_e32 v117, v117, v46
	s_waitcnt lgkmcnt(4)
	v_add_f32_e32 v117, v117, v47
	s_waitcnt lgkmcnt(3)
	v_add_f32_e32 v117, v117, v48
	s_waitcnt lgkmcnt(2)
	v_add_f32_e32 v117, v117, v49
	s_waitcnt lgkmcnt(1)
	v_add_f32_e32 v117, v117, v50
	s_waitcnt lgkmcnt(0)
	v_add_f32_e32 v117, v117, v51
	ds_read_b32 v36, v112 offset:18432
	ds_read_b32 v37, v112 offset:19584
	ds_read_b32 v38, v112 offset:20736
	ds_read_b32 v39, v112 offset:21888
	ds_read_b32 v40, v112 offset:23040
	ds_read_b32 v41, v112 offset:24192
	ds_read_b32 v42, v112 offset:25344
	ds_read_b32 v43, v112 offset:26496
	ds_read_b32 v44, v112 offset:27648
	ds_read_b32 v45, v112 offset:28800
	ds_read_b32 v46, v112 offset:29952
	ds_read_b32 v47, v112 offset:31104
	ds_read_b32 v48, v112 offset:32256
	ds_read_b32 v49, v112 offset:33408
	ds_read_b32 v50, v112 offset:34560
	ds_read_b32 v51, v112 offset:35712
	s_waitcnt lgkmcnt(15)
	v_add_f32_e32 v117, v117, v36
	s_waitcnt lgkmcnt(14)
	v_add_f32_e32 v117, v117, v37
	s_waitcnt lgkmcnt(13)
	v_add_f32_e32 v117, v117, v38
	s_waitcnt lgkmcnt(12)
	v_add_f32_e32 v117, v117, v39
	s_waitcnt lgkmcnt(11)
	v_add_f32_e32 v117, v117, v40
	s_waitcnt lgkmcnt(10)
	v_add_f32_e32 v117, v117, v41
	s_waitcnt lgkmcnt(9)
	v_add_f32_e32 v117, v117, v42
	s_waitcnt lgkmcnt(8)
	v_add_f32_e32 v117, v117, v43
	s_waitcnt lgkmcnt(7)
	v_add_f32_e32 v117, v117, v44
	s_waitcnt lgkmcnt(6)
	v_add_f32_e32 v117, v117, v45
	s_waitcnt lgkmcnt(5)
	v_add_f32_e32 v117, v117, v46
	s_waitcnt lgkmcnt(4)
	v_add_f32_e32 v117, v117, v47
	s_waitcnt lgkmcnt(3)
	v_add_f32_e32 v117, v117, v48
	s_waitcnt lgkmcnt(2)
	v_add_f32_e32 v117, v117, v49
	s_waitcnt lgkmcnt(1)
	v_add_f32_e32 v117, v117, v50
	s_waitcnt lgkmcnt(0)
	v_add_f32_e32 v117, v117, v51
	ds_read_b32 v36, v113 offset:0
	ds_read_b32 v37, v113 offset:1152
	ds_read_b32 v38, v113 offset:2304
	ds_read_b32 v39, v113 offset:3456
	ds_read_b32 v40, v113 offset:4608
	ds_read_b32 v41, v113 offset:5760
	ds_read_b32 v42, v113 offset:6912
	ds_read_b32 v43, v113 offset:8064
	ds_read_b32 v44, v113 offset:9216
	ds_read_b32 v45, v113 offset:10368
	ds_read_b32 v46, v113 offset:11520
	ds_read_b32 v47, v113 offset:12672
	ds_read_b32 v48, v113 offset:13824
	ds_read_b32 v49, v113 offset:14976
	ds_read_b32 v50, v113 offset:16128
	ds_read_b32 v51, v113 offset:17280
	s_waitcnt lgkmcnt(15)
	v_add_f32_e32 v117, v117, v36
	s_waitcnt lgkmcnt(14)
	v_add_f32_e32 v117, v117, v37
	s_waitcnt lgkmcnt(13)
	v_add_f32_e32 v117, v117, v38
	s_waitcnt lgkmcnt(12)
	v_add_f32_e32 v117, v117, v39
	s_waitcnt lgkmcnt(11)
	v_add_f32_e32 v117, v117, v40
	s_waitcnt lgkmcnt(10)
	v_add_f32_e32 v117, v117, v41
	s_waitcnt lgkmcnt(9)
	v_add_f32_e32 v117, v117, v42
	s_waitcnt lgkmcnt(8)
	v_add_f32_e32 v117, v117, v43
	s_waitcnt lgkmcnt(7)
	v_add_f32_e32 v117, v117, v44
	s_waitcnt lgkmcnt(6)
	v_add_f32_e32 v117, v117, v45
	s_waitcnt lgkmcnt(5)
	v_add_f32_e32 v117, v117, v46
	s_waitcnt lgkmcnt(4)
	v_add_f32_e32 v117, v117, v47
	s_waitcnt lgkmcnt(3)
	v_add_f32_e32 v117, v117, v48
	s_waitcnt lgkmcnt(2)
	v_add_f32_e32 v117, v117, v49
	s_waitcnt lgkmcnt(1)
	v_add_f32_e32 v117, v117, v50
	s_waitcnt lgkmcnt(0)
	v_add_f32_e32 v117, v117, v51
	ds_read_b32 v36, v113 offset:18432
	ds_read_b32 v37, v113 offset:19584
	ds_read_b32 v38, v113 offset:20736
	ds_read_b32 v39, v113 offset:21888
	ds_read_b32 v40, v113 offset:23040
	ds_read_b32 v41, v113 offset:24192
	ds_read_b32 v42, v113 offset:25344
	ds_read_b32 v43, v113 offset:26496
	ds_read_b32 v44, v113 offset:27648
	ds_read_b32 v45, v113 offset:28800
	ds_read_b32 v46, v113 offset:29952
	ds_read_b32 v47, v113 offset:31104
	ds_read_b32 v48, v113 offset:32256
	ds_read_b32 v49, v113 offset:33408
	ds_read_b32 v50, v113 offset:34560
	ds_read_b32 v51, v113 offset:35712
	s_waitcnt lgkmcnt(15)
	v_add_f32_e32 v117, v117, v36
	s_waitcnt lgkmcnt(14)
	v_add_f32_e32 v117, v117, v37
	s_waitcnt lgkmcnt(13)
	v_add_f32_e32 v117, v117, v38
	s_waitcnt lgkmcnt(12)
	v_add_f32_e32 v117, v117, v39
	s_waitcnt lgkmcnt(11)
	v_add_f32_e32 v117, v117, v40
	s_waitcnt lgkmcnt(10)
	v_add_f32_e32 v117, v117, v41
	s_waitcnt lgkmcnt(9)
	v_add_f32_e32 v117, v117, v42
	s_waitcnt lgkmcnt(8)
	v_add_f32_e32 v117, v117, v43
	s_waitcnt lgkmcnt(7)
	v_add_f32_e32 v117, v117, v44
	s_waitcnt lgkmcnt(6)
	v_add_f32_e32 v117, v117, v45
	s_waitcnt lgkmcnt(5)
	v_add_f32_e32 v117, v117, v46
	s_waitcnt lgkmcnt(4)
	v_add_f32_e32 v117, v117, v47
	s_waitcnt lgkmcnt(3)
	v_add_f32_e32 v117, v117, v48
	s_waitcnt lgkmcnt(2)
	v_add_f32_e32 v117, v117, v49
	s_waitcnt lgkmcnt(1)
	v_add_f32_e32 v117, v117, v50
	s_waitcnt lgkmcnt(0)
	v_add_f32_e32 v117, v117, v51
	s_waitcnt vmcnt(16)
	v_add_f32_e32 v117, v117, v115
	global_store_dword v114, v117, s[30:31]
	s_barrier
	s_add_i32 s4, s4, 1
	s_cmp_lt_u32 s4, 3
	s_cbranch_scc1 .Lada_item
	s_waitcnt vmcnt(0)
	s_barrier
